# speedup vs baseline: 1.0024x; 1.0006x over previous
.Lep1_prej:
	s_waitcnt lgkmcnt(7)
	s_barrier
	s_cmp_eq_u64 s[6:7], 0
	s_cbranch_scc0 .Lep1_k1
	s_mul_i32 s43, s36, 0x5000
	s_add_i32 s43, s43, s86
	s_add_u32 s40, s18, s43
	s_addc_u32 s41, s19, 0
	ds_read2st64_b32 v[50:51], v221 offset0:0 offset1:1
	ds_read2st64_b32 v[52:53], v221 offset0:2 offset1:3
	ds_read2st64_b32 v[54:55], v221 offset0:4 offset1:5
	ds_read2st64_b32 v[56:57], v221 offset0:6 offset1:7
	ds_read2st64_b32 v[58:59], v221 offset0:8 offset1:9
	ds_read2st64_b32 v[60:61], v221 offset0:10 offset1:11
	s_waitcnt lgkmcnt(12)
	v_fma_f32 v78, -v76, v77, 0
	s_waitcnt lgkmcnt(4)
	v_pk_add_f32 v[34:35], v[34:35], v[50:51]
	v_pk_add_f32 v[36:37], v[36:37], v[52:53]
	v_pk_add_f32 v[34:35], v[34:35], v[78:79] op_sel_hi:[1,0]
	v_pk_add_f32 v[36:37], v[36:37], v[78:79] op_sel_hi:[1,0]
	v_pk_fma_f32 v[34:35], v[62:63], v[76:77], v[34:35] op_sel:[0,1,0] op_sel_hi:[1,1,1]
	v_pk_fma_f32 v[36:37], v[64:65], v[76:77], v[36:37] op_sel:[0,1,0] op_sel_hi:[1,1,1]
	v_pk_mul_f32 v[20:21], v[34:35], v[34:35]
	v_pk_add_f32 v[18:19], v[34:35], v[36:37]
	v_pk_fma_f32 v[20:21], v[36:37], v[36:37], v[20:21]
	s_waitcnt lgkmcnt(2)
	v_pk_add_f32 v[38:39], v[38:39], v[54:55]
	v_pk_add_f32 v[40:41], v[40:41], v[56:57]
	v_pk_add_f32 v[38:39], v[38:39], v[78:79] op_sel_hi:[1,0]
	v_pk_add_f32 v[40:41], v[40:41], v[78:79] op_sel_hi:[1,0]
	v_pk_fma_f32 v[38:39], v[68:69], v[76:77], v[38:39] op_sel:[0,1,0] op_sel_hi:[1,1,1]
	v_pk_fma_f32 v[40:41], v[70:71], v[76:77], v[40:41] op_sel:[0,1,0] op_sel_hi:[1,1,1]
	v_pk_add_f32 v[18:19], v[18:19], v[38:39]
	v_pk_fma_f32 v[20:21], v[38:39], v[38:39], v[20:21]
	v_pk_add_f32 v[18:19], v[18:19], v[40:41]
	v_pk_fma_f32 v[20:21], v[40:41], v[40:41], v[20:21]
	s_waitcnt lgkmcnt(0)
	v_pk_add_f32 v[42:43], v[42:43], v[58:59]
	v_pk_add_f32 v[44:45], v[44:45], v[60:61]
	v_pk_add_f32 v[42:43], v[42:43], v[78:79] op_sel_hi:[1,0]
	v_pk_add_f32 v[44:45], v[44:45], v[78:79] op_sel_hi:[1,0]
	v_pk_fma_f32 v[42:43], v[72:73], v[76:77], v[42:43] op_sel:[0,1,0] op_sel_hi:[1,1,1]
	v_pk_fma_f32 v[44:45], v[74:75], v[76:77], v[44:45] op_sel:[0,1,0] op_sel_hi:[1,1,1]
	v_pk_add_f32 v[18:19], v[18:19], v[42:43]
	v_pk_fma_f32 v[20:21], v[42:43], v[42:43], v[20:21]
	v_pk_add_f32 v[18:19], v[18:19], v[44:45]
	v_pk_fma_f32 v[20:21], v[44:45], v[44:45], v[20:21]
	ds_read2st64_b32 v[50:51], v221 offset0:12 offset1:13
	ds_read2st64_b32 v[52:53], v221 offset0:14 offset1:15
	ds_read2st64_b32 v[54:55], v221 offset0:16 offset1:17
	ds_read2st64_b32 v[56:57], v221 offset0:18 offset1:19
	ds_read2st64_b32 v[58:59], v221 offset0:20 offset1:21
	ds_read2st64_b32 v[60:61], v221 offset0:22 offset1:23
	ds_read2st64_b32 v[62:63], v67 offset0:48 offset1:50
	ds_read2st64_b32 v[64:65], v67 offset0:52 offset1:54
	ds_read2st64_b32 v[68:69], v67 offset0:64 offset1:66
	ds_read2st64_b32 v[70:71], v67 offset0:68 offset1:70
	ds_read2st64_b32 v[72:73], v67 offset0:80 offset1:82
	ds_read2st64_b32 v[74:75], v67 offset0:84 offset1:86
	s_waitcnt lgkmcnt(4)
	v_pk_add_f32 v[46:47], v[46:47], v[50:51]
	v_pk_add_f32 v[48:49], v[48:49], v[52:53]
	v_pk_add_f32 v[46:47], v[46:47], v[78:79] op_sel_hi:[1,0]
	v_pk_add_f32 v[48:49], v[48:49], v[78:79] op_sel_hi:[1,0]
	v_pk_fma_f32 v[46:47], v[62:63], v[76:77], v[46:47] op_sel:[0,1,0] op_sel_hi:[1,1,1]
	v_pk_fma_f32 v[48:49], v[64:65], v[76:77], v[48:49] op_sel:[0,1,0] op_sel_hi:[1,1,1]
	v_pk_add_f32 v[18:19], v[18:19], v[46:47]
	v_pk_fma_f32 v[20:21], v[46:47], v[46:47], v[20:21]
	v_pk_add_f32 v[18:19], v[18:19], v[48:49]
	v_pk_fma_f32 v[20:21], v[48:49], v[48:49], v[20:21]
	s_barrier
	ds_read_b32 v80, v236
	s_waitcnt lgkmcnt(3)
	v_pk_add_f32 v[2:3], v[2:3], v[54:55]
	v_pk_add_f32 v[4:5], v[4:5], v[56:57]
	v_pk_add_f32 v[2:3], v[2:3], v[78:79] op_sel_hi:[1,0]
	v_pk_add_f32 v[4:5], v[4:5], v[78:79] op_sel_hi:[1,0]
	v_pk_fma_f32 v[2:3], v[68:69], v[76:77], v[2:3] op_sel:[0,1,0] op_sel_hi:[1,1,1]
	v_pk_fma_f32 v[4:5], v[70:71], v[76:77], v[4:5] op_sel:[0,1,0] op_sel_hi:[1,1,1]
	v_pk_add_f32 v[18:19], v[18:19], v[2:3]
	v_pk_fma_f32 v[20:21], v[2:3], v[2:3], v[20:21]
	v_pk_add_f32 v[18:19], v[18:19], v[4:5]
	v_pk_fma_f32 v[20:21], v[4:5], v[4:5], v[20:21]
	s_waitcnt lgkmcnt(1)
	v_pk_add_f32 v[6:7], v[6:7], v[58:59]
	v_pk_add_f32 v[8:9], v[8:9], v[60:61]
	v_pk_add_f32 v[6:7], v[6:7], v[78:79] op_sel_hi:[1,0]
	v_pk_add_f32 v[8:9], v[8:9], v[78:79] op_sel_hi:[1,0]
	v_pk_fma_f32 v[6:7], v[72:73], v[76:77], v[6:7] op_sel:[0,1,0] op_sel_hi:[1,1,1]
	v_pk_fma_f32 v[8:9], v[74:75], v[76:77], v[8:9] op_sel:[0,1,0] op_sel_hi:[1,1,1]
	v_pk_add_f32 v[18:19], v[18:19], v[6:7]
	v_pk_fma_f32 v[20:21], v[6:7], v[6:7], v[20:21]
	v_pk_add_f32 v[18:19], v[18:19], v[8:9]
	v_pk_fma_f32 v[20:21], v[8:9], v[8:9], v[20:21]
	v_add_f32_e32 v18, v18, v19
	v_add_f32_e32 v20, v20, v21
	s_nop 1
	v_permlane32_swap_b32_e32 v18, v20
	v_add_f32_e32 v22, v18, v20
	s_branch .Lep1_wr0

.Lep2_prej:
	s_waitcnt lgkmcnt(7)
	s_barrier
	s_cmp_eq_u64 s[6:7], 0
	s_cbranch_scc0 .Lep2_k1
	s_mul_i32 s43, s36, 0x5000
	s_addk_i32 s43, 0x2800
	s_add_i32 s43, s43, s86
	s_add_u32 s40, s18, s43
	s_addc_u32 s41, s19, 0
	ds_read2st64_b32 v[50:51], v221 offset0:0 offset1:1
	ds_read2st64_b32 v[52:53], v221 offset0:2 offset1:3
	ds_read2st64_b32 v[54:55], v221 offset0:4 offset1:5
	ds_read2st64_b32 v[56:57], v221 offset0:6 offset1:7
	ds_read2st64_b32 v[58:59], v221 offset0:8 offset1:9
	ds_read2st64_b32 v[60:61], v221 offset0:10 offset1:11
	s_waitcnt lgkmcnt(12)
	v_fma_f32 v78, -v76, v77, v173
	s_waitcnt lgkmcnt(4)
	v_pk_add_f32 v[34:35], v[34:35], v[50:51]
	v_pk_add_f32 v[36:37], v[36:37], v[52:53]
	v_pk_add_f32 v[34:35], v[34:35], v[78:79] op_sel_hi:[1,0]
	v_pk_add_f32 v[36:37], v[36:37], v[78:79] op_sel_hi:[1,0]
	v_pk_fma_f32 v[34:35], v[62:63], v[76:77], v[34:35] op_sel:[0,1,0] op_sel_hi:[1,1,1]
	v_pk_fma_f32 v[36:37], v[64:65], v[76:77], v[36:37] op_sel:[0,1,0] op_sel_hi:[1,1,1]
	v_pk_mul_f32 v[20:21], v[34:35], v[34:35]
	v_pk_add_f32 v[18:19], v[34:35], v[36:37]
	v_pk_fma_f32 v[20:21], v[36:37], v[36:37], v[20:21]
	s_waitcnt lgkmcnt(2)
	v_pk_add_f32 v[38:39], v[38:39], v[54:55]
	v_pk_add_f32 v[40:41], v[40:41], v[56:57]
	v_pk_add_f32 v[38:39], v[38:39], v[78:79] op_sel_hi:[1,0]
	v_pk_add_f32 v[40:41], v[40:41], v[78:79] op_sel_hi:[1,0]
	v_pk_fma_f32 v[38:39], v[68:69], v[76:77], v[38:39] op_sel:[0,1,0] op_sel_hi:[1,1,1]
	v_pk_fma_f32 v[40:41], v[70:71], v[76:77], v[40:41] op_sel:[0,1,0] op_sel_hi:[1,1,1]
	v_pk_add_f32 v[18:19], v[18:19], v[38:39]
	v_pk_fma_f32 v[20:21], v[38:39], v[38:39], v[20:21]
	v_pk_add_f32 v[18:19], v[18:19], v[40:41]
	v_pk_fma_f32 v[20:21], v[40:41], v[40:41], v[20:21]
	s_waitcnt lgkmcnt(0)
	v_pk_add_f32 v[42:43], v[42:43], v[58:59]
	v_pk_add_f32 v[44:45], v[44:45], v[60:61]
	v_pk_add_f32 v[42:43], v[42:43], v[78:79] op_sel_hi:[1,0]
	v_pk_add_f32 v[44:45], v[44:45], v[78:79] op_sel_hi:[1,0]
	v_pk_fma_f32 v[42:43], v[72:73], v[76:77], v[42:43] op_sel:[0,1,0] op_sel_hi:[1,1,1]
	v_pk_fma_f32 v[44:45], v[74:75], v[76:77], v[44:45] op_sel:[0,1,0] op_sel_hi:[1,1,1]
	v_pk_add_f32 v[18:19], v[18:19], v[42:43]
	v_pk_fma_f32 v[20:21], v[42:43], v[42:43], v[20:21]
	v_pk_add_f32 v[18:19], v[18:19], v[44:45]
	v_pk_fma_f32 v[20:21], v[44:45], v[44:45], v[20:21]
	ds_read2st64_b32 v[50:51], v221 offset0:12 offset1:13
	ds_read2st64_b32 v[52:53], v221 offset0:14 offset1:15
	ds_read2st64_b32 v[54:55], v221 offset0:16 offset1:17
	ds_read2st64_b32 v[56:57], v221 offset0:18 offset1:19
	ds_read2st64_b32 v[58:59], v221 offset0:20 offset1:21
	ds_read2st64_b32 v[60:61], v221 offset0:22 offset1:23
	ds_read2st64_b32 v[62:63], v67 offset0:48 offset1:50
	ds_read2st64_b32 v[64:65], v67 offset0:52 offset1:54
	ds_read2st64_b32 v[68:69], v67 offset0:64 offset1:66
	ds_read2st64_b32 v[70:71], v67 offset0:68 offset1:70
	ds_read2st64_b32 v[72:73], v67 offset0:80 offset1:82
	ds_read2st64_b32 v[74:75], v67 offset0:84 offset1:86
	s_waitcnt lgkmcnt(4)
	v_pk_add_f32 v[46:47], v[46:47], v[50:51]
	v_pk_add_f32 v[48:49], v[48:49], v[52:53]
	v_pk_add_f32 v[46:47], v[46:47], v[78:79] op_sel_hi:[1,0]
	v_pk_add_f32 v[48:49], v[48:49], v[78:79] op_sel_hi:[1,0]
	v_pk_fma_f32 v[46:47], v[62:63], v[76:77], v[46:47] op_sel:[0,1,0] op_sel_hi:[1,1,1]
	v_pk_fma_f32 v[48:49], v[64:65], v[76:77], v[48:49] op_sel:[0,1,0] op_sel_hi:[1,1,1]
	v_pk_add_f32 v[18:19], v[18:19], v[46:47]
	v_pk_fma_f32 v[20:21], v[46:47], v[46:47], v[20:21]
	v_pk_add_f32 v[18:19], v[18:19], v[48:49]
	v_pk_fma_f32 v[20:21], v[48:49], v[48:49], v[20:21]
	s_barrier
	ds_read_b32 v80, v236
	s_waitcnt lgkmcnt(3)
	v_pk_add_f32 v[2:3], v[2:3], v[54:55]
	v_pk_add_f32 v[4:5], v[4:5], v[56:57]
	v_pk_add_f32 v[2:3], v[2:3], v[78:79] op_sel_hi:[1,0]
	v_pk_add_f32 v[4:5], v[4:5], v[78:79] op_sel_hi:[1,0]
	v_pk_fma_f32 v[2:3], v[68:69], v[76:77], v[2:3] op_sel:[0,1,0] op_sel_hi:[1,1,1]
	v_pk_fma_f32 v[4:5], v[70:71], v[76:77], v[4:5] op_sel:[0,1,0] op_sel_hi:[1,1,1]
	v_pk_add_f32 v[18:19], v[18:19], v[2:3]
	v_pk_fma_f32 v[20:21], v[2:3], v[2:3], v[20:21]
	v_pk_add_f32 v[18:19], v[18:19], v[4:5]
	v_pk_fma_f32 v[20:21], v[4:5], v[4:5], v[20:21]
	s_waitcnt lgkmcnt(1)
	v_pk_add_f32 v[6:7], v[6:7], v[58:59]
	v_pk_add_f32 v[8:9], v[8:9], v[60:61]
	v_pk_add_f32 v[6:7], v[6:7], v[78:79] op_sel_hi:[1,0]
	v_pk_add_f32 v[8:9], v[8:9], v[78:79] op_sel_hi:[1,0]
	v_pk_fma_f32 v[6:7], v[72:73], v[76:77], v[6:7] op_sel:[0,1,0] op_sel_hi:[1,1,1]
	v_pk_fma_f32 v[8:9], v[74:75], v[76:77], v[8:9] op_sel:[0,1,0] op_sel_hi:[1,1,1]
	v_pk_add_f32 v[18:19], v[18:19], v[6:7]
	v_pk_fma_f32 v[20:21], v[6:7], v[6:7], v[20:21]
	v_pk_add_f32 v[18:19], v[18:19], v[8:9]
	v_pk_fma_f32 v[20:21], v[8:9], v[8:9], v[20:21]
	v_add_f32_e32 v18, v18, v19
	v_add_f32_e32 v20, v20, v21
	s_nop 1
	v_permlane32_swap_b32_e32 v18, v20
	v_add_f32_e32 v22, v18, v20
	s_branch .Lep2_wr0
